# c3
# speedup vs baseline: 1.0204x; 1.0092x over previous
.LBB2_88:
	s_or_b64 exec, exec, s[10:11]
	v_mov_b32_e32 v33, v24
	v_mov_b32_e32 v24, v25
	v_mov_b32_e32 v25, v26
	v_pk_add_f32 v[184:185], v[68:69], v[24:25]
	v_mov_b32_e32 v24, v82
	v_mov_b32_e32 v25, v70
	v_mov_b32_e32 v26, v55
	v_pk_add_f32 v[180:181], v[24:25], v[26:27]
	v_mov_b32_e32 v24, v83
	v_mov_b32_e32 v25, v84
	v_mov_b32_e32 v32, v23
	v_pk_add_f32 v[186:187], v[24:25], v[56:57]
	v_mov_b32_e32 v24, v85
	v_mov_b32_e32 v25, v86
	v_pk_add_f32 v[182:183], v[66:67], v[32:33]
	v_pk_add_f32 v[188:189], v[24:25], v[58:59]
	s_waitcnt lgkmcnt(1)
	v_mfma_f32_32x32x16_f16 v[2:17], v[116:119], v[60:63], v[2:17]
	s_waitcnt lgkmcnt(0)
	v_mfma_f32_32x32x16_f16 v[2:17], v[112:115], v[28:31], v[2:17]
	s_mul_i32 s2, s2, s40
	s_bfe_u32 s28, s42, 0x30003
	s_add_i32 s2, s2, s41
	s_lshl_b32 s10, s28, 17
	s_and_b32 s2, s2, 7
	s_add_i32 s10, s33, s10
	s_nop 5
	v_mov_b32_e32 v17, 15
	s_lshl_b32 s2, s2, 12
	v_lshlrev_b32_sdwa v17, v17, v193 dst_sel:DWORD dst_unused:UNUSED_PAD src0_sel:DWORD src1_sel:BYTE_1
	v_add_lshl_u32 v23, v192, v191, 10
	s_add_i32 s2, s2, s10
	v_add3_u32 v17, s2, v17, v23
	s_movk_i32 s10, 0xfc00
	v_add3_u32 v24, v17, v1, s10
	v_ashrrev_i32_e32 v25, 31, v24
	v_lshl_add_u64 v[26:27], v[24:25], 2, s[14:15]
	v_lshlrev_b64 v[192:193], 4, v[24:25]
	v_lshlrev_b32_e32 v23, 15, v195
	v_add_lshl_u32 v24, v196, v194, 10
	v_add3_u32 v23, s2, v23, v24
	s_mov_b32 s29, 0xffff7c00
	v_add3_u32 v24, v23, v1, s29
	s_mov_b64 s[10:11], 0x280
	v_ashrrev_i32_e32 v25, 31, v24
	v_lshl_add_u64 v[32:33], v[26:27], 0, s[10:11]
	v_lshl_add_u64 v[26:27], v[24:25], 2, s[14:15]
	v_lshlrev_b64 v[196:197], 4, v[24:25]
	v_lshlrev_b32_e32 v24, 15, v198
	v_add_lshl_u32 v25, v64, v191, 10
	v_add3_u32 v28, s2, v24, v25
	v_add3_u32 v24, v28, v1, s29
	v_add_u32_e32 v217, 0xfffffc80, v17
	s_lshl_b32 s2, s28, 7
	v_lshlrev_b32_e32 v17, 5, v214
	v_ashrrev_i32_e32 v25, 31, v24
	v_or3_b32 v17, v190, s2, v17
	v_lshl_add_u64 v[194:195], v[26:27], 0, s[10:11]
	v_lshl_add_u64 v[26:27], v[24:25], 2, s[14:15]
	v_add3_u32 v17, v17, s3, v213
	s_mov_b32 s40, 2
	v_lshl_add_u64 v[198:199], v[26:27], 0, s[10:11]
	v_lshlrev_b64 v[200:201], 4, v[24:25]
	v_add_u32_e32 v215, 0xffff7c80, v28
	v_add_u32_e32 v216, 0xffff7c80, v23
	v_lshl_add_u32 v213, v17, 10, s33
	s_mov_b64 s[10:11], 0x100
	v_mov_b32_e32 v230, 0
	v_mov_b32_e32 v231, 0
	v_mov_b32_e32 v232, 0
	v_mov_b32_e32 v233, 0
	v_mov_b32_e32 v234, 0
	v_mov_b32_e32 v235, 0
	v_mov_b32_e32 v236, 0
	v_mov_b32_e32 v237, 0
	v_mov_b32_e32 v238, 0
	v_mov_b32_e32 v239, 0
	s_barrier

.LBB2_104:
	s_or_b64 exec, exec, s[34:35]
	s_waitcnt lgkmcnt(3)
	v_mfma_f32_32x32x16_f16 v[56:71], v[128:131], v[92:95], v[56:71]
	v_mfma_f32_32x32x16_f16 v[72:87], v[132:135], v[92:95], v[72:87]
	ds_read_b128 v[92:95], v205 offset:15840
	ds_read_b128 v[28:31], v207 offset:15840
	s_waitcnt lgkmcnt(4)
	v_mfma_f32_32x32x16_f16 v[56:71], v[124:127], v[12:15], v[56:71]
	v_mfma_f32_32x32x16_f16 v[72:87], v[108:111], v[12:15], v[72:87]
	s_waitcnt lgkmcnt(3)
	s_and_saveexec_b64 s[34:35], s[8:9]
	s_cbranch_execz .LBB2_109
	s_mov_b64 s[38:39], s[26:27]
	ds_write_b128 v211, v[24:27] offset:38032
	ds_write_b32 v211, v17 offset:38564
	s_and_saveexec_b64 s[36:37], s[4:5]
	s_andn2_b64 s[38:39], s[26:27], exec
	s_and_b64 s[42:43], s[6:7], exec
	s_or_b64 s[38:39], s[38:39], s[42:43]
	ds_write_b32 v211, v17 offset:38552
	s_or_b64 exec, exec, s[36:37]
	s_and_b64 exec, exec, s[38:39]
	ds_write_b32 v211, v17 offset:38576
.LBB2_109:
	s_or_b64 exec, exec, s[34:35]
	s_waitcnt lgkmcnt(0)
	s_barrier
	ds_read_b128 v[24:27], v205 offset:38016
	ds_read_b128 v[12:15], v205 offset:39072
	v_mfma_f32_32x32x16_f16 v[56:71], v[116:119], v[88:91], v[56:71]
	v_mfma_f32_32x32x16_f16 v[72:87], v[128:131], v[88:91], v[72:87]
	v_mfma_f32_32x32x16_f16 v[56:71], v[112:115], v[44:47], v[56:71]
	v_mfma_f32_32x32x16_f16 v[72:87], v[124:127], v[44:47], v[72:87]
	v_mfma_f32_32x32x16_f16 v[72:87], v[116:119], v[92:95], v[72:87]
	v_mfma_f32_32x32x16_f16 v[72:87], v[112:115], v[28:31], v[72:87]
	s_waitcnt lgkmcnt(1)
	v_mfma_f32_32x32x16_f16 v[88:103], v[176:179], v[24:27], 0
	ds_read_b128 v[24:27], v207 offset:38016
	ds_read_b128 v[184:187], v205 offset:40128
	ds_read_b128 v[188:191], v207 offset:39072
	ds_read_b128 v[180:183], v207 offset:40128
	s_waitcnt lgkmcnt(3)
	v_mfma_f32_32x32x16_f16 v[88:103], v[172:175], v[24:27], v[88:103]
	s_and_saveexec_b64 s[34:35], s[28:29]
	s_cbranch_execz .LBB2_111
	v_lshl_add_u64 v[16:17], s[20:21], 0, v[200:201]
	global_load_dwordx4 v[232:235], v[16:17], off offset:2560
	global_load_dword v230, v[198:199], off

.LBB2_115:
	s_or_b64 exec, exec, s[28:29]
	v_add_f32_e32 v49, v19, v40
	v_add_f32_e32 v55, v20, v41
	v_add_f32_e32 v54, v54, v11
	v_add_f32_e32 v39, v18, v39
	v_add_f32_e32 v222, v21, v42
	v_add_f32_e32 v223, v22, v43
	v_add_f32_e32 v7, v50, v7
	v_add_f32_e32 v224, v51, v8
	v_add_f32_e32 v225, v52, v9
	v_add_f32_e32 v226, v53, v10
	v_mfma_f32_32x32x16_f16 v[88:103], v[168:171], v[12:15], v[88:103]
	ds_read_b128 v[40:43], v205 offset:41184
	ds_read_b128 v[50:53], v207 offset:41184
	v_mfma_f32_32x32x16_f16 v[240:255], v[176:179], v[12:15], 0
	s_waitcnt lgkmcnt(3)
	v_mfma_f32_32x32x16_f16 v[88:103], v[160:163], v[188:191], v[88:103]
	v_mfma_f32_32x32x16_f16 v[240:255], v[172:175], v[188:191], v[240:255]
	v_mfma_f32_32x32x16_f16 v[88:103], v[164:167], v[184:187], v[88:103]
	v_mfma_f32_32x32x16_f16 v[240:255], v[168:171], v[184:187], v[240:255]
	ds_read_b128 v[184:187], v205 offset:44352
	ds_read_b128 v[188:191], v207 offset:44352
	s_waitcnt lgkmcnt(4)
	v_mfma_f32_32x32x16_f16 v[88:103], v[156:159], v[180:183], v[88:103]
	v_mfma_f32_32x32x16_f16 v[240:255], v[160:163], v[180:183], v[240:255]
	v_add_f32_e32 v84, v225, v84
	v_add_f32_e32 v85, v226, v85
	s_waitcnt lgkmcnt(3)
	v_mfma_f32_32x32x16_f16 v[240:255], v[164:167], v[40:43], v[240:255]
	v_add_f32_e32 v40, 0, v85
	v_max_f32_e32 v84, 0, v84
	v_max_f32_e32 v40, 0, v40
	v_cvt_pk_f16_f32 v43, v84, v40
	v_add_f32_e32 v7, v7, v82
	v_add_f32_e32 v40, v224, v83
	v_max_f32_e32 v7, 0, v7
	v_max_f32_e32 v40, 0, v40
	v_cvt_pk_f16_f32 v42, v7, v40
	v_add_f32_e32 v40, v55, v68
	v_add_f32_e32 v41, v222, v69
	v_max_f32_e32 v40, 0, v40
	v_max_f32_e32 v41, 0, v41
	s_waitcnt lgkmcnt(2)
	v_mfma_f32_32x32x16_f16 v[240:255], v[156:159], v[50:53], v[240:255]
	v_cvt_pk_f16_f32 v41, v40, v41
	v_add_f32_e32 v39, v39, v66
	v_add_f32_e32 v40, v49, v67
	v_max_f32_e32 v39, 0, v39
	v_max_f32_e32 v40, 0, v40
	ds_read_b128 v[180:183], v205 offset:45408
	ds_read_b128 v[218:221], v207 offset:45408
	v_add_f32_e32 v7, v54, v86
	v_cvt_pk_f16_f32 v40, v39, v40
	v_add_f32_e32 v39, v223, v70
	v_add_u32_e32 v48, 64, v48
	v_max_f32_e32 v7, 0, v7
	v_max_f32_e32 v39, 0, v39
	v_ashrrev_i32_e32 v49, 31, v48
	v_permlane32_swap_b32_e32 v40, v42
	v_permlane32_swap_b32_e32 v41, v43
	v_permlane32_swap_b32_e32 v39, v7
	v_lshl_add_u64 v[50:51], v[48:49], 4, s[16:17]
	global_store_dwordx4 v[50:51], v[40:43], off sc1
	v_cvt_pk_f16_f32 v7, v39, v7
	s_nop 0
	v_lshl_add_u64 v[40:41], v[48:49], 2, s[18:19]
	global_store_dword v[40:41], v7, off sc1
	s_waitcnt lgkmcnt(3)
	v_mfma_f32_32x32x16_f16 v[88:103], v[136:139], v[184:187], v[88:103]
	ds_read_b128 v[52:55], v205 offset:46464
	ds_read_b128 v[66:69], v207 offset:46464
	s_waitcnt lgkmcnt(4)
	v_mfma_f32_32x32x16_f16 v[88:103], v[140:143], v[188:191], v[88:103]
	s_waitcnt lgkmcnt(3)
	v_mfma_f32_32x32x16_f16 v[88:103], v[120:123], v[180:183], v[88:103]
	ds_read_b128 v[48:51], v205 offset:47520
	ds_read_b128 v[40:43], v207 offset:47520
	v_mfma_f32_32x32x16_f16 v[240:255], v[136:139], v[180:183], v[240:255]
	s_waitcnt lgkmcnt(4)
	v_mfma_f32_32x32x16_f16 v[88:103], v[152:155], v[218:221], v[88:103]
	v_mfma_f32_32x32x16_f16 v[240:255], v[140:143], v[218:221], v[240:255]
	s_waitcnt lgkmcnt(3)
	v_mfma_f32_32x32x16_f16 v[88:103], v[148:151], v[52:55], v[88:103]
	s_mov_b64 s[2:3], s[26:27]
	v_mfma_f32_32x32x16_f16 v[240:255], v[120:123], v[52:55], v[240:255]
	ds_read_b128 v[52:55], v205 offset:50688
	ds_read_b128 v[82:85], v207 offset:50688
	s_waitcnt vmcnt(3)
	ds_write_b128 v208, v[232:235] offset:16
	s_waitcnt vmcnt(2)
	ds_write_b32 v208, v230 offset:548
	s_waitcnt lgkmcnt(6)
	v_mfma_f32_32x32x16_f16 v[88:103], v[144:147], v[66:69], v[88:103]
	v_mfma_f32_32x32x16_f16 v[240:255], v[152:155], v[66:69], v[240:255]
	s_and_saveexec_b64 s[28:29], s[4:5]
	s_andn2_b64 s[2:3], s[26:27], exec
	s_and_b64 s[30:31], s[6:7], exec
	s_or_b64 s[2:3], s[2:3], s[30:31]
	ds_write_b32 v208, v230 offset:536
	s_or_b64 exec, exec, s[28:29]
	s_and_saveexec_b64 s[28:29], s[2:3]
	ds_write_b32 v208, v230 offset:560
	s_or_b64 exec, exec, s[28:29]
	s_waitcnt lgkmcnt(5)
	v_mfma_f32_32x32x16_f16 v[240:255], v[148:151], v[48:51], v[240:255]
	ds_read_b128 v[66:69], v205 offset:51744
	ds_read_b128 v[44:47], v207 offset:51744
	s_waitcnt lgkmcnt(6)
	v_mfma_f32_32x32x16_f16 v[240:255], v[144:147], v[40:43], v[240:255]
	s_waitcnt lgkmcnt(5)
	v_mfma_f32_32x32x16_f16 v[88:103], v[132:135], v[52:55], v[88:103]
	ds_read_b128 v[52:55], v205 offset:52800
	ds_read_b128 v[48:51], v207 offset:52800
	s_waitcnt lgkmcnt(6)
	v_mfma_f32_32x32x16_f16 v[88:103], v[108:111], v[82:85], v[88:103]
	s_and_saveexec_b64 s[2:3], s[0:1]
	s_cbranch_execz .LBB2_124
	s_mov_b64 s[30:31], s[26:27]
	ds_write_b128 v210, v[236:239] offset:16
	ds_write_b32 v210, v231 offset:548
	s_and_saveexec_b64 s[28:29], s[4:5]
	s_andn2_b64 s[30:31], s[26:27], exec
	s_and_b64 s[34:35], s[6:7], exec
	s_or_b64 s[30:31], s[30:31], s[34:35]
	ds_write_b32 v210, v231 offset:536
	s_or_b64 exec, exec, s[28:29]
	s_and_b64 exec, exec, s[30:31]
	ds_write_b32 v210, v231 offset:560
.LBB2_124:
	s_or_b64 exec, exec, s[2:3]
	s_waitcnt lgkmcnt(3)
	v_mfma_f32_32x32x16_f16 v[88:103], v[128:131], v[66:69], v[88:103]
	ds_read_b128 v[40:43], v205 offset:53856
	ds_read_b128 v[28:31], v207 offset:53856
	v_mfma_f32_32x32x16_f16 v[240:255], v[132:135], v[66:69], v[240:255]
	s_waitcnt lgkmcnt(4)
	v_mfma_f32_32x32x16_f16 v[88:103], v[124:127], v[44:47], v[88:103]
	v_mfma_f32_32x32x16_f16 v[240:255], v[108:111], v[44:47], v[240:255]
	s_waitcnt lgkmcnt(3)
	v_mfma_f32_32x32x16_f16 v[88:103], v[116:119], v[52:55], v[88:103]
	v_mfma_f32_32x32x16_f16 v[240:255], v[128:131], v[52:55], v[240:255]
	s_waitcnt lgkmcnt(2)
	v_mfma_f32_32x32x16_f16 v[88:103], v[112:115], v[48:51], v[88:103]
	v_mfma_f32_32x32x16_f16 v[240:255], v[124:127], v[48:51], v[240:255]
	s_and_saveexec_b64 s[2:3], s[8:9]
	s_cbranch_execz .LBB2_129
	s_mov_b64 s[30:31], s[26:27]
	ds_write_b128 v211, v[24:27] offset:16
	ds_write_b32 v211, v87 offset:548
	s_and_saveexec_b64 s[28:29], s[4:5]
	s_andn2_b64 s[30:31], s[26:27], exec
	s_and_b64 s[34:35], s[6:7], exec
	s_or_b64 s[30:31], s[30:31], s[34:35]
	ds_write_b32 v211, v87 offset:536
	s_or_b64 exec, exec, s[28:29]
	s_and_b64 exec, exec, s[30:31]
	ds_write_b32 v211, v87 offset:560
.LBB2_129:
	s_or_b64 exec, exec, s[2:3]
	v_mov_b32_e32 v24, v61
	v_mov_b32_e32 v25, v62
	v_pk_add_f32 v[182:183], v[34:35], v[24:25]
	v_mov_b32_e32 v24, v63
	v_mov_b32_e32 v25, v64
	v_pk_add_f32 v[184:185], v[36:37], v[24:25]
	v_mov_b32_e32 v24, v2
	v_mov_b32_e32 v2, v3
	v_mov_b32_e32 v3, v4
	v_mov_b32_e32 v25, v38
	v_mov_b32_e32 v64, v77
	v_pk_add_f32 v[186:187], v[2:3], v[78:79]
	v_mov_b32_e32 v2, v5
	v_mov_b32_e32 v3, v6
	v_pk_add_f32 v[180:181], v[24:25], v[64:65]
	v_pk_add_f32 v[188:189], v[2:3], v[80:81]
	s_waitcnt lgkmcnt(1)
	v_mfma_f32_32x32x16_f16 v[240:255], v[116:119], v[40:43], v[240:255]
	s_waitcnt lgkmcnt(0)
	v_mfma_f32_32x32x16_f16 v[2:17], v[112:115], v[28:31], v[240:255]
	s_add_u32 s20, s20, 0x400
	s_addc_u32 s21, s21, 0
	v_lshl_add_u64 v[32:33], v[32:33], 0, s[10:11]
	v_lshl_add_u64 v[194:195], v[194:195], 0, s[10:11]
	v_lshl_add_u64 v[198:199], v[198:199], 0, s[10:11]
	v_add_u32_e32 v215, 64, v215
	v_add_u32_e32 v216, 64, v216
	v_add_u32_e32 v217, 64, v217
	s_cmp_lt_u32 s40, 30
	v_add_u32_e32 v213, 64, v213
	s_barrier
	s_cbranch_scc0 .LBB2_131
	v_mov_b64_e32 v[34:35], v[88:89]
	v_mov_b32_e32 v54, v76
	v_mov_b32_e32 v53, v75
	v_mov_b32_e32 v52, v74
	v_mov_b32_e32 v51, v73
	v_mov_b32_e32 v50, v72
	v_mov_b32_e32 v22, v60
	v_mov_b32_e32 v21, v59
	v_mov_b32_e32 v20, v58
	v_mov_b32_e32 v19, v57
	v_mov_b32_e32 v18, v56
	v_mov_b64_e32 v[36:37], v[90:91]
	v_mov_b64_e32 v[38:39], v[92:93]
	v_mov_b64_e32 v[40:41], v[94:95]
	v_mov_b64_e32 v[42:43], v[96:97]
	v_mov_b64_e32 v[44:45], v[98:99]
	v_mov_b64_e32 v[46:47], v[100:101]
	v_mov_b64_e32 v[48:49], v[102:103]
	s_branch .LBB2_89

	.amdhsa_kernel _Z7k2_mfmaPK15HIP_vector_typeIjLj4EEPKjS2_PKfPS0_Pj
		.amdhsa_group_segment_fixed_size 0
		.amdhsa_private_segment_fixed_size 0
		.amdhsa_kernarg_size 304
		.amdhsa_user_sgpr_count 2
		.amdhsa_user_sgpr_dispatch_ptr 0
		.amdhsa_user_sgpr_queue_ptr 0
		.amdhsa_user_sgpr_kernarg_segment_ptr 1
		.amdhsa_user_sgpr_dispatch_id 0
		.amdhsa_user_sgpr_kernarg_preload_length 0
		.amdhsa_user_sgpr_kernarg_preload_offset 0
		.amdhsa_user_sgpr_private_segment_size 0
		.amdhsa_uses_dynamic_stack 0
		.amdhsa_enable_private_segment 0
		.amdhsa_system_sgpr_workgroup_id_x 1
		.amdhsa_system_sgpr_workgroup_id_y 0
		.amdhsa_system_sgpr_workgroup_id_z 0
		.amdhsa_system_sgpr_workgroup_info 0
		.amdhsa_system_vgpr_workitem_id 0
		.amdhsa_next_free_vgpr 256
		.amdhsa_next_free_sgpr 46
		.amdhsa_accum_offset 256
		.amdhsa_reserve_vcc 1
		.amdhsa_float_round_mode_32 0
		.amdhsa_float_round_mode_16_64 0
		.amdhsa_float_denorm_mode_32 3
		.amdhsa_float_denorm_mode_16_64 3
		.amdhsa_dx10_clamp 1
		.amdhsa_ieee_mode 1
		.amdhsa_fp16_overflow 0
		.amdhsa_tg_split 0
		.amdhsa_exception_fp_ieee_invalid_op 0
		.amdhsa_exception_fp_denorm_src 0
		.amdhsa_exception_fp_ieee_div_zero 0
		.amdhsa_exception_fp_ieee_overflow 0
		.amdhsa_exception_fp_ieee_underflow 0
		.amdhsa_exception_fp_ieee_inexact 0
		.amdhsa_exception_int_div_zero 0
	.end_amdhsa_kernel

.LBB6_532:
	s_or_b64 exec, exec, s[34:35]
	v_mfma_f32_32x32x16_f16 v[56:71], v[164:167], v[72:75], v[56:71]
	ds_read_b128 v[218:221], v209 offset:3168
	ds_read_b128 v[222:225], v211 offset:3168
	v_mfma_f32_32x32x16_f16 v[72:87], v[176:179], v[72:75], 0
	s_waitcnt lgkmcnt(3)
	v_mfma_f32_32x32x16_f16 v[56:71], v[160:163], v[100:103], v[56:71]
	v_mfma_f32_32x32x16_f16 v[72:87], v[172:175], v[100:103], v[72:87]
	v_mfma_f32_32x32x16_f16 v[56:71], v[168:171], v[96:99], v[56:71]
	v_mfma_f32_32x32x16_f16 v[72:87], v[164:167], v[96:99], v[72:87]
	ds_read_b128 v[96:99], v209 offset:6336
	ds_read_b128 v[100:103], v211 offset:6336
	s_waitcnt lgkmcnt(4)
	v_mfma_f32_32x32x16_f16 v[56:71], v[156:159], v[92:95], v[56:71]
	v_mfma_f32_32x32x16_f16 v[72:87], v[160:163], v[92:95], v[72:87]
	v_add_f32_e32 v14, v187, v14
	v_add_f32_e32 v15, v188, v15
	s_waitcnt lgkmcnt(3)
	v_mfma_f32_32x32x16_f16 v[72:87], v[168:171], v[218:221], v[72:87]
	v_add_f32_e32 v12, v180, v12
	v_add_f32_e32 v13, v186, v13
	v_max_f32_e32 v14, 0, v14
	v_max_f32_e32 v15, 0, v15
	v_max_f32_e32 v12, 0, v12
	v_max_f32_e32 v13, 0, v13
	v_cvt_pk_f16_f32 v15, v14, v15
	v_cvt_pk_f16_f32 v14, v12, v13
	v_add_f32_e32 v12, v189, v16
	v_max_f32_e32 v16, 0, v12
	v_add_f32_e32 v12, v184, v46
	v_add_f32_e32 v13, v185, v47
	v_max_f32_e32 v12, 0, v12
	v_max_f32_e32 v13, 0, v13
	s_waitcnt lgkmcnt(2)
	v_mfma_f32_32x32x16_f16 v[72:87], v[156:159], v[222:225], v[72:87]
	v_cvt_pk_f16_f32 v13, v12, v13
	v_add_f32_e32 v12, v182, v44
	v_add_f32_e32 v44, v183, v45
	v_max_f32_e32 v12, 0, v12
	v_max_f32_e32 v44, 0, v44
	ds_read_b128 v[92:95], v209 offset:7392
	ds_read_b128 v[226:229], v211 offset:7392
	v_cvt_pk_f16_f32 v12, v12, v44
	v_add_f32_e32 v44, v181, v48
	v_max_f32_e32 v46, 0, v44
	v_permlane32_swap_b32_e32 v12, v14
	v_permlane32_swap_b32_e32 v13, v15
	v_permlane32_swap_b32_e32 v46, v16
	v_lshl_add_u64 v[44:45], s[20:21], 0, v[200:201]
	global_store_dwordx4 v[44:45], v[12:15], off sc1
	s_nop 1
	v_cvt_pk_f16_f32 v12, v46, v16
	global_store_dword v[198:199], v12, off sc1
	s_waitcnt lgkmcnt(3)
	v_mfma_f32_32x32x16_f16 v[56:71], v[132:135], v[96:99], v[56:71]
	ds_read_b128 v[96:99], v209 offset:8448
	ds_read_b128 v[180:183], v211 offset:8448
	s_waitcnt lgkmcnt(4)
	v_mfma_f32_32x32x16_f16 v[56:71], v[140:143], v[100:103], v[56:71]
	s_waitcnt lgkmcnt(3)
	v_mfma_f32_32x32x16_f16 v[56:71], v[120:123], v[92:95], v[56:71]
	ds_read_b128 v[12:15], v209 offset:9504
	ds_read_b128 v[44:47], v211 offset:9504
	v_mfma_f32_32x32x16_f16 v[72:87], v[132:135], v[92:95], v[72:87]
	s_waitcnt lgkmcnt(4)
	v_mfma_f32_32x32x16_f16 v[56:71], v[152:155], v[226:229], v[56:71]
	v_mfma_f32_32x32x16_f16 v[72:87], v[140:143], v[226:229], v[72:87]
	s_waitcnt lgkmcnt(3)
	v_mfma_f32_32x32x16_f16 v[56:71], v[148:151], v[96:99], v[56:71]
	s_mov_b64 s[34:35], s[26:27]
	v_mfma_f32_32x32x16_f16 v[72:87], v[120:123], v[96:99], v[72:87]
	ds_read_b128 v[100:103], v209 offset:12672
	ds_read_b128 v[96:99], v211 offset:12672
	s_waitcnt vmcnt(3)
	ds_write_b128 v212, v[88:91] offset:38032
	s_waitcnt vmcnt(2)
	ds_write_b32 v212, v49 offset:38564
	s_waitcnt lgkmcnt(6)
	v_mfma_f32_32x32x16_f16 v[56:71], v[144:147], v[180:183], v[56:71]
	v_mfma_f32_32x32x16_f16 v[72:87], v[152:155], v[180:183], v[72:87]
	s_and_saveexec_b64 s[36:37], s[4:5]
	s_andn2_b64 s[34:35], s[26:27], exec
	s_and_b64 s[38:39], s[6:7], exec
	s_or_b64 s[34:35], s[34:35], s[38:39]
	ds_write_b32 v212, v49 offset:38552
	s_or_b64 exec, exec, s[36:37]
	s_and_saveexec_b64 s[36:37], s[34:35]
	ds_write_b32 v212, v49 offset:38576
	s_or_b64 exec, exec, s[36:37]
	s_waitcnt lgkmcnt(5)
	v_mfma_f32_32x32x16_f16 v[72:87], v[148:151], v[12:15], v[72:87]
	ds_read_b128 v[92:95], v209 offset:13728
	ds_read_b128 v[12:15], v211 offset:13728
	s_waitcnt lgkmcnt(6)
	v_mfma_f32_32x32x16_f16 v[72:87], v[144:147], v[44:47], v[72:87]
	s_waitcnt lgkmcnt(5)
	v_mfma_f32_32x32x16_f16 v[56:71], v[136:139], v[100:103], v[56:71]
	ds_read_b128 v[88:91], v209 offset:14784
	ds_read_b128 v[44:47], v211 offset:14784
	s_waitcnt lgkmcnt(6)
	v_mfma_f32_32x32x16_f16 v[56:71], v[108:111], v[96:99], v[56:71]
	s_and_saveexec_b64 s[34:35], s[0:1]
	s_cbranch_execz .LBB6_541
	s_mov_b64 s[38:39], s[26:27]
	ds_write_b128 v214, v[28:31] offset:38032
	ds_write_b32 v214, v23 offset:38564
	s_and_saveexec_b64 s[36:37], s[4:5]
	s_andn2_b64 s[38:39], s[26:27], exec
	s_and_b64 s[42:43], s[6:7], exec
	s_or_b64 s[38:39], s[38:39], s[42:43]
	ds_write_b32 v214, v23 offset:38552
	s_or_b64 exec, exec, s[36:37]
	s_and_b64 exec, exec, s[38:39]
	ds_write_b32 v214, v23 offset:38576
.LBB6_541:
	s_or_b64 exec, exec, s[34:35]
	s_waitcnt lgkmcnt(3)
	v_mfma_f32_32x32x16_f16 v[56:71], v[128:131], v[92:95], v[56:71]
	v_mfma_f32_32x32x16_f16 v[72:87], v[136:139], v[92:95], v[72:87]
	ds_read_b128 v[92:95], v209 offset:15840
	ds_read_b128 v[28:31], v211 offset:15840
	s_waitcnt lgkmcnt(4)
	v_mfma_f32_32x32x16_f16 v[56:71], v[124:127], v[12:15], v[56:71]
	v_mfma_f32_32x32x16_f16 v[72:87], v[108:111], v[12:15], v[72:87]
	s_waitcnt lgkmcnt(3)
	s_and_saveexec_b64 s[34:35], s[8:9]
	s_cbranch_execz .LBB6_546
	s_mov_b64 s[38:39], s[26:27]
	ds_write_b128 v215, v[24:27] offset:38032
	ds_write_b32 v215, v17 offset:38564
	s_and_saveexec_b64 s[36:37], s[4:5]
	s_andn2_b64 s[38:39], s[26:27], exec
	s_and_b64 s[42:43], s[6:7], exec
	s_or_b64 s[38:39], s[38:39], s[42:43]
	ds_write_b32 v215, v17 offset:38552
	s_or_b64 exec, exec, s[36:37]
	s_and_b64 exec, exec, s[38:39]
	ds_write_b32 v215, v17 offset:38576
.LBB6_546:
	s_or_b64 exec, exec, s[34:35]
	s_waitcnt lgkmcnt(0)
	s_barrier
	ds_read_b128 v[24:27], v209 offset:38016
	ds_read_b128 v[12:15], v209 offset:39072
	v_mfma_f32_32x32x16_f16 v[56:71], v[116:119], v[88:91], v[56:71]
	v_mfma_f32_32x32x16_f16 v[72:87], v[128:131], v[88:91], v[72:87]
	v_mfma_f32_32x32x16_f16 v[56:71], v[112:115], v[44:47], v[56:71]
	v_mfma_f32_32x32x16_f16 v[72:87], v[124:127], v[44:47], v[72:87]
	v_mfma_f32_32x32x16_f16 v[72:87], v[116:119], v[92:95], v[72:87]
	v_mfma_f32_32x32x16_f16 v[72:87], v[112:115], v[28:31], v[72:87]
	s_waitcnt lgkmcnt(1)
	v_mfma_f32_32x32x16_f16 v[88:103], v[176:179], v[24:27], 0
	ds_read_b128 v[24:27], v211 offset:38016
	ds_read_b128 v[184:187], v209 offset:40128
	ds_read_b128 v[188:191], v211 offset:39072
	ds_read_b128 v[180:183], v211 offset:40128
	v_mov_b32_e32 v71, 0
	s_nop 1
	v_mov_b32_e32 v87, 0
	v_mov_b32_e32 v44, 0
	v_mov_b32_e32 v45, 0
	v_mov_b32_e32 v46, 0
	v_mov_b32_e32 v47, 0
	s_waitcnt lgkmcnt(3)
	v_mfma_f32_32x32x16_f16 v[88:103], v[172:175], v[24:27], v[88:103]
	s_and_saveexec_b64 s[34:35], s[28:29]
	s_cbranch_execz .LBB6_548
	v_lshl_add_u64 v[16:17], v[32:33], 4, s[12:13]
	global_load_dwordx4 v[44:47], v[16:17], off offset:512
	v_lshl_add_u64 v[16:17], v[32:33], 2, s[14:15]
	global_load_dword v87, v[16:17], off offset:128

.LBB6_552:
	s_or_b64 exec, exec, s[28:29]
	v_add_f32_e32 v39, v18, v39
	v_add_f32_e32 v202, v19, v40
	v_add_f32_e32 v203, v20, v41
	v_add_f32_e32 v204, v21, v42
	v_add_f32_e32 v205, v22, v43
	v_add_f32_e32 v7, v50, v7
	v_add_f32_e32 v218, v51, v8
	v_add_f32_e32 v219, v52, v9
	v_add_f32_e32 v220, v53, v10
	v_add_f32_e32 v221, v54, v11
	v_mfma_f32_32x32x16_f16 v[88:103], v[164:167], v[12:15], v[88:103]
	ds_read_b128 v[40:43], v209 offset:41184
	ds_read_b128 v[48:51], v211 offset:41184
	v_mfma_f32_32x32x16_f16 v[240:255], v[176:179], v[12:15], 0
	s_waitcnt lgkmcnt(3)
	v_mfma_f32_32x32x16_f16 v[88:103], v[160:163], v[188:191], v[88:103]
	v_mfma_f32_32x32x16_f16 v[240:255], v[172:175], v[188:191], v[240:255]
	v_mfma_f32_32x32x16_f16 v[88:103], v[168:171], v[184:187], v[88:103]
	v_mfma_f32_32x32x16_f16 v[240:255], v[164:167], v[184:187], v[240:255]
	ds_read_b128 v[52:55], v209 offset:44352
	ds_read_b128 v[184:187], v211 offset:44352
	s_waitcnt lgkmcnt(4)
	v_mfma_f32_32x32x16_f16 v[88:103], v[156:159], v[180:183], v[88:103]
	v_mfma_f32_32x32x16_f16 v[240:255], v[160:163], v[180:183], v[240:255]
	v_add_f32_e32 v84, v219, v84
	v_add_f32_e32 v85, v220, v85
	s_waitcnt lgkmcnt(3)
	v_mfma_f32_32x32x16_f16 v[240:255], v[168:171], v[40:43], v[240:255]
	v_add_f32_e32 v40, 0, v85
	v_max_f32_e32 v84, 0, v84
	v_max_f32_e32 v40, 0, v40
	v_cvt_pk_f16_f32 v43, v84, v40
	v_add_f32_e32 v7, v7, v82
	v_add_f32_e32 v40, v218, v83
	v_max_f32_e32 v7, 0, v7
	v_max_f32_e32 v40, 0, v40
	v_cvt_pk_f16_f32 v42, v7, v40
	v_add_f32_e32 v40, v203, v68
	v_add_f32_e32 v41, v204, v69
	v_max_f32_e32 v40, 0, v40
	v_max_f32_e32 v41, 0, v41
	s_waitcnt lgkmcnt(2)
	v_mfma_f32_32x32x16_f16 v[240:255], v[156:159], v[48:51], v[240:255]
	v_cvt_pk_f16_f32 v41, v40, v41
	v_add_f32_e32 v39, v39, v66
	v_add_f32_e32 v40, v202, v67
	v_max_f32_e32 v39, 0, v39
	v_max_f32_e32 v40, 0, v40
	ds_read_b128 v[180:183], v209 offset:45408
	ds_read_b128 v[188:191], v211 offset:45408
	v_add_f32_e32 v7, v221, v86
	v_cvt_pk_f16_f32 v40, v39, v40
	v_add_f32_e32 v39, v205, v70
	v_max_f32_e32 v7, 0, v7
	v_max_f32_e32 v39, 0, v39
	s_nop 1
	v_permlane32_swap_b32_e32 v39, v7
	v_permlane32_swap_b32_e32 v40, v42
	v_permlane32_swap_b32_e32 v41, v43
	v_lshl_add_u64 v[48:49], s[20:21], 0, v[194:195]
	v_cvt_pk_f16_f32 v7, v39, v7
	global_store_dwordx4 v[48:49], v[40:43], off offset:1024 sc1
	global_store_dword v[196:197], v7, off sc1
	s_waitcnt lgkmcnt(3)
	v_mfma_f32_32x32x16_f16 v[88:103], v[132:135], v[52:55], v[88:103]
	ds_read_b128 v[52:55], v209 offset:46464
	ds_read_b128 v[66:69], v211 offset:46464
	s_waitcnt lgkmcnt(4)
	v_mfma_f32_32x32x16_f16 v[88:103], v[140:143], v[184:187], v[88:103]
	s_waitcnt lgkmcnt(3)
	v_mfma_f32_32x32x16_f16 v[88:103], v[120:123], v[180:183], v[88:103]
	ds_read_b128 v[48:51], v209 offset:47520
	ds_read_b128 v[40:43], v211 offset:47520
	v_mfma_f32_32x32x16_f16 v[240:255], v[132:135], v[180:183], v[240:255]
	s_waitcnt lgkmcnt(4)
	v_mfma_f32_32x32x16_f16 v[88:103], v[152:155], v[188:191], v[88:103]
	v_mfma_f32_32x32x16_f16 v[240:255], v[140:143], v[188:191], v[240:255]
	s_waitcnt lgkmcnt(3)
	v_mfma_f32_32x32x16_f16 v[88:103], v[148:151], v[52:55], v[88:103]
	s_mov_b64 s[2:3], s[26:27]
	v_mfma_f32_32x32x16_f16 v[240:255], v[120:123], v[52:55], v[240:255]
	ds_read_b128 v[52:55], v209 offset:50688
	ds_read_b128 v[82:85], v211 offset:50688
	s_waitcnt vmcnt(3)
	ds_write_b128 v212, v[44:47] offset:16
	s_waitcnt vmcnt(2)
	ds_write_b32 v212, v87 offset:548
	s_waitcnt lgkmcnt(6)
	v_mfma_f32_32x32x16_f16 v[88:103], v[144:147], v[66:69], v[88:103]
	v_mfma_f32_32x32x16_f16 v[240:255], v[152:155], v[66:69], v[240:255]
	s_and_saveexec_b64 s[28:29], s[4:5]
	s_andn2_b64 s[2:3], s[26:27], exec
	s_and_b64 s[30:31], s[6:7], exec
	s_or_b64 s[2:3], s[2:3], s[30:31]
	ds_write_b32 v212, v87 offset:536
	s_or_b64 exec, exec, s[28:29]
	s_and_saveexec_b64 s[28:29], s[2:3]
	ds_write_b32 v212, v87 offset:560
	s_or_b64 exec, exec, s[28:29]
	s_waitcnt lgkmcnt(5)
	v_mfma_f32_32x32x16_f16 v[240:255], v[148:151], v[48:51], v[240:255]
	ds_read_b128 v[66:69], v209 offset:51744
	ds_read_b128 v[44:47], v211 offset:51744
	s_waitcnt lgkmcnt(6)
	v_mfma_f32_32x32x16_f16 v[240:255], v[144:147], v[40:43], v[240:255]
	s_waitcnt lgkmcnt(5)
	v_mfma_f32_32x32x16_f16 v[88:103], v[136:139], v[52:55], v[88:103]
	ds_read_b128 v[52:55], v209 offset:52800
	ds_read_b128 v[48:51], v211 offset:52800
	s_waitcnt lgkmcnt(6)
	v_mfma_f32_32x32x16_f16 v[88:103], v[108:111], v[82:85], v[88:103]
	s_and_saveexec_b64 s[2:3], s[0:1]
	s_cbranch_execz .LBB6_561
	s_mov_b64 s[30:31], s[26:27]
	ds_write_b128 v214, v[28:31] offset:16
	ds_write_b32 v214, v71 offset:548
	s_and_saveexec_b64 s[28:29], s[4:5]
	s_andn2_b64 s[30:31], s[26:27], exec
	s_and_b64 s[34:35], s[6:7], exec
	s_or_b64 s[30:31], s[30:31], s[34:35]
	ds_write_b32 v214, v71 offset:536
	s_or_b64 exec, exec, s[28:29]
	s_and_b64 exec, exec, s[30:31]
	ds_write_b32 v214, v71 offset:560
.LBB6_561:
	s_or_b64 exec, exec, s[2:3]
	s_waitcnt lgkmcnt(3)
	v_mfma_f32_32x32x16_f16 v[88:103], v[128:131], v[66:69], v[88:103]
	ds_read_b128 v[40:43], v209 offset:53856
	ds_read_b128 v[28:31], v211 offset:53856
	v_mfma_f32_32x32x16_f16 v[240:255], v[136:139], v[66:69], v[240:255]
	s_waitcnt lgkmcnt(4)
	v_mfma_f32_32x32x16_f16 v[88:103], v[124:127], v[44:47], v[88:103]
	v_mfma_f32_32x32x16_f16 v[240:255], v[108:111], v[44:47], v[240:255]
	s_waitcnt lgkmcnt(3)
	v_mfma_f32_32x32x16_f16 v[88:103], v[116:119], v[52:55], v[88:103]
	v_mfma_f32_32x32x16_f16 v[240:255], v[128:131], v[52:55], v[240:255]
	s_waitcnt lgkmcnt(2)
	v_mfma_f32_32x32x16_f16 v[88:103], v[112:115], v[48:51], v[88:103]
	v_mfma_f32_32x32x16_f16 v[240:255], v[124:127], v[48:51], v[240:255]
	s_and_saveexec_b64 s[2:3], s[8:9]
	s_cbranch_execz .LBB6_566
	s_mov_b64 s[30:31], s[26:27]
	ds_write_b128 v215, v[24:27] offset:16
	ds_write_b32 v215, v32 offset:548
	s_and_saveexec_b64 s[28:29], s[4:5]
	s_andn2_b64 s[30:31], s[26:27], exec
	s_and_b64 s[34:35], s[6:7], exec
	s_or_b64 s[30:31], s[30:31], s[34:35]
	ds_write_b32 v215, v32 offset:536
	s_or_b64 exec, exec, s[28:29]
	s_and_b64 exec, exec, s[30:31]
	ds_write_b32 v215, v32 offset:560
.LBB6_566:
	s_or_b64 exec, exec, s[2:3]
	v_mov_b32_e32 v24, v61
	v_mov_b32_e32 v25, v62
	v_pk_add_f32 v[182:183], v[34:35], v[24:25]
	v_mov_b32_e32 v24, v63
	v_mov_b32_e32 v25, v64
	v_pk_add_f32 v[184:185], v[36:37], v[24:25]
	v_mov_b32_e32 v24, v2
	v_mov_b32_e32 v2, v3
	v_mov_b32_e32 v3, v4
	v_mov_b32_e32 v25, v38
	v_mov_b32_e32 v64, v77
	v_pk_add_f32 v[186:187], v[2:3], v[78:79]
	v_mov_b32_e32 v2, v5
	v_mov_b32_e32 v3, v6
	v_pk_add_f32 v[180:181], v[24:25], v[64:65]
	v_pk_add_f32 v[188:189], v[2:3], v[80:81]
	s_waitcnt lgkmcnt(1)
	v_mfma_f32_32x32x16_f16 v[240:255], v[116:119], v[40:43], v[240:255]
	s_waitcnt lgkmcnt(0)
	v_mfma_f32_32x32x16_f16 v[2:17], v[112:115], v[28:31], v[240:255]
	s_add_u32 s20, s20, 0x400
	s_addc_u32 s21, s21, 0
	v_add_u32_e32 v193, 64, v193
	v_add_u32_e32 v216, 64, v216
	v_add_u32_e32 v217, 64, v217
	v_lshl_add_u64 v[196:197], v[196:197], 0, s[10:11]
	s_cmp_lt_u32 s33, 30
	v_lshl_add_u64 v[198:199], v[198:199], 0, s[10:11]
	s_barrier
	s_cbranch_scc0 .LBB6_568
	v_mov_b64_e32 v[34:35], v[88:89]
	v_mov_b32_e32 v54, v76
	v_mov_b32_e32 v53, v75
	v_mov_b32_e32 v52, v74
	v_mov_b32_e32 v51, v73
	v_mov_b32_e32 v50, v72
	v_mov_b32_e32 v22, v60
	v_mov_b32_e32 v21, v59
	v_mov_b32_e32 v20, v58
	v_mov_b32_e32 v19, v57
	v_mov_b32_e32 v18, v56
	v_mov_b64_e32 v[36:37], v[90:91]
	v_mov_b64_e32 v[38:39], v[92:93]
	v_mov_b64_e32 v[40:41], v[94:95]
	v_mov_b64_e32 v[42:43], v[96:97]
	v_mov_b64_e32 v[44:45], v[98:99]
	v_mov_b64_e32 v[46:47], v[100:101]
	v_mov_b64_e32 v[48:49], v[102:103]
	s_branch .LBB6_526

	.amdhsa_kernel _Z8k23_mfmaPK15HIP_vector_typeIjLj4EEPKjS2_PKfPS0_PjS2_S4_S2_S6_Pf
		.amdhsa_group_segment_fixed_size 0
		.amdhsa_private_segment_fixed_size 0
		.amdhsa_kernarg_size 88
		.amdhsa_user_sgpr_count 2
		.amdhsa_user_sgpr_dispatch_ptr 0
		.amdhsa_user_sgpr_queue_ptr 0
		.amdhsa_user_sgpr_kernarg_segment_ptr 1
		.amdhsa_user_sgpr_dispatch_id 0
		.amdhsa_user_sgpr_kernarg_preload_length 0
		.amdhsa_user_sgpr_kernarg_preload_offset 0
		.amdhsa_user_sgpr_private_segment_size 0
		.amdhsa_uses_dynamic_stack 0
		.amdhsa_enable_private_segment 0
		.amdhsa_system_sgpr_workgroup_id_x 1
		.amdhsa_system_sgpr_workgroup_id_y 0
		.amdhsa_system_sgpr_workgroup_id_z 0
		.amdhsa_system_sgpr_workgroup_info 0
		.amdhsa_system_vgpr_workitem_id 0
		.amdhsa_next_free_vgpr 256
		.amdhsa_next_free_sgpr 66
		.amdhsa_accum_offset 256
		.amdhsa_reserve_vcc 1
		.amdhsa_float_round_mode_32 0
		.amdhsa_float_round_mode_16_64 0
		.amdhsa_float_denorm_mode_32 3
		.amdhsa_float_denorm_mode_16_64 3
		.amdhsa_dx10_clamp 1
		.amdhsa_ieee_mode 1
		.amdhsa_fp16_overflow 0
		.amdhsa_tg_split 0
		.amdhsa_exception_fp_ieee_invalid_op 0
		.amdhsa_exception_fp_denorm_src 0
		.amdhsa_exception_fp_ieee_div_zero 0
		.amdhsa_exception_fp_ieee_overflow 0
		.amdhsa_exception_fp_ieee_underflow 0
		.amdhsa_exception_fp_ieee_inexact 0
		.amdhsa_exception_int_div_zero 0
	.end_amdhsa_kernel

amdhsa.kernels:
  - .agpr_count:     0
    .args:
      - .actual_access:  read_only
        .address_space:  global
        .offset:         0
        .size:           8
        .value_kind:     global_buffer
      - .actual_access:  read_only
        .address_space:  global
        .offset:         8
        .size:           8
        .value_kind:     global_buffer
      - .actual_access:  read_only
        .address_space:  global
        .offset:         16
        .size:           8
        .value_kind:     global_buffer
      - .actual_access:  write_only
        .address_space:  global
        .offset:         24
        .size:           8
        .value_kind:     global_buffer
      - .actual_access:  write_only
        .address_space:  global
        .offset:         32
        .size:           8
        .value_kind:     global_buffer
    .group_segment_fixed_size: 6520
    .kernarg_segment_align: 8
    .kernarg_segment_size: 40
    .language:       OpenCL C
    .language_version:
      - 2
      - 0
    .max_flat_workgroup_size: 256
    .name:           _Z8k1_naivePKfS0_S0_P15HIP_vector_typeIjLj4EEPj
    .private_segment_fixed_size: 0
    .sgpr_count:     30
    .sgpr_spill_count: 0
    .symbol:         _Z8k1_naivePKfS0_S0_P15HIP_vector_typeIjLj4EEPj.kd
    .uniform_work_group_size: 1
    .uses_dynamic_stack: false
    .vgpr_count:     40
    .vgpr_spill_count: 0
    .wavefront_size: 64
  - .agpr_count:     0
    .args:
      - .actual_access:  read_only
        .address_space:  global
        .offset:         0
        .size:           8
        .value_kind:     global_buffer
      - .actual_access:  read_only
        .address_space:  global
        .offset:         8
        .size:           8
        .value_kind:     global_buffer
      - .actual_access:  read_only
        .address_space:  global
        .offset:         16
        .size:           8
        .value_kind:     global_buffer
      - .actual_access:  read_only
        .address_space:  global
        .offset:         24
        .size:           8
        .value_kind:     global_buffer
      - .actual_access:  write_only
        .address_space:  global
        .offset:         32
        .size:           8
        .value_kind:     global_buffer
      - .actual_access:  write_only
        .address_space:  global
        .offset:         40
        .size:           8
        .value_kind:     global_buffer
      - .offset:         48
        .size:           4
        .value_kind:     by_value
    .group_segment_fixed_size: 32448
    .kernarg_segment_align: 8
    .kernarg_segment_size: 52
    .language:       OpenCL C
    .language_version:
      - 2
      - 0
    .max_flat_workgroup_size: 256
    .name:           _Z8k2_naivePK15HIP_vector_typeIjLj4EEPKjPKfS6_PS0_Pji
    .private_segment_fixed_size: 0
    .sgpr_count:     30
    .sgpr_spill_count: 0
    .symbol:         _Z8k2_naivePK15HIP_vector_typeIjLj4EEPKjPKfS6_PS0_Pji.kd
    .uniform_work_group_size: 1
    .uses_dynamic_stack: false
    .vgpr_count:     102
    .vgpr_spill_count: 0
    .wavefront_size: 64
  - .agpr_count:     0
    .args:
      - .actual_access:  read_only
        .address_space:  global
        .offset:         0
        .size:           8
        .value_kind:     global_buffer
      - .actual_access:  read_only
        .address_space:  global
        .offset:         8
        .size:           8
        .value_kind:     global_buffer
      - .actual_access:  read_only
        .address_space:  global
        .offset:         16
        .size:           8
        .value_kind:     global_buffer
      - .actual_access:  read_only
        .address_space:  global
        .offset:         24
        .size:           8
        .value_kind:     global_buffer
      - .actual_access:  write_only
        .address_space:  global
        .offset:         32
        .size:           8
        .value_kind:     global_buffer
      - .actual_access:  write_only
        .address_space:  global
        .offset:         40
        .size:           8
        .value_kind:     global_buffer
      - .offset:         48
        .size:           4
        .value_kind:     hidden_block_count_x
      - .offset:         52
        .size:           4
        .value_kind:     hidden_block_count_y
      - .offset:         56
        .size:           4
        .value_kind:     hidden_block_count_z
      - .offset:         60
        .size:           2
        .value_kind:     hidden_group_size_x
      - .offset:         62
        .size:           2
        .value_kind:     hidden_group_size_y
      - .offset:         64
        .size:           2
        .value_kind:     hidden_group_size_z
      - .offset:         66
        .size:           2
        .value_kind:     hidden_remainder_x
      - .offset:         68
        .size:           2
        .value_kind:     hidden_remainder_y
      - .offset:         70
        .size:           2
        .value_kind:     hidden_remainder_z
      - .offset:         88
        .size:           8
        .value_kind:     hidden_global_offset_x
      - .offset:         96
        .size:           8
        .value_kind:     hidden_global_offset_y
      - .offset:         104
        .size:           8
        .value_kind:     hidden_global_offset_z
      - .offset:         112
        .size:           2
        .value_kind:     hidden_grid_dims
      - .offset:         168
        .size:           4
        .value_kind:     hidden_dynamic_lds_size
    .group_segment_fixed_size: 0
    .kernarg_segment_align: 8
    .kernarg_segment_size: 304
    .language:       OpenCL C
    .language_version:
      - 2
      - 0
    .max_flat_workgroup_size: 512
    .name:           _Z7k2_mfmaPK15HIP_vector_typeIjLj4EEPKjS2_PKfPS0_Pj
    .private_segment_fixed_size: 0
    .sgpr_count:     52
    .sgpr_spill_count: 0
    .symbol:         _Z7k2_mfmaPK15HIP_vector_typeIjLj4EEPKjS2_PKfPS0_Pj.kd
    .uniform_work_group_size: 1
    .uses_dynamic_stack: false
    .vgpr_count:     256
    .vgpr_spill_count: 0
    .wavefront_size: 64
  - .agpr_count:     0
    .args:
      - .actual_access:  read_only
        .address_space:  global
        .offset:         0
        .size:           8
        .value_kind:     global_buffer
      - .actual_access:  write_only
        .address_space:  global
        .offset:         8
        .size:           8
        .value_kind:     global_buffer
      - .offset:         16
        .size:           4
        .value_kind:     hidden_block_count_x
      - .offset:         20
        .size:           4
        .value_kind:     hidden_block_count_y
      - .offset:         24
        .size:           4
        .value_kind:     hidden_block_count_z
      - .offset:         28
        .size:           2
        .value_kind:     hidden_group_size_x
      - .offset:         30
        .size:           2
        .value_kind:     hidden_group_size_y
      - .offset:         32
        .size:           2
        .value_kind:     hidden_group_size_z
      - .offset:         34
        .size:           2
        .value_kind:     hidden_remainder_x
      - .offset:         36
        .size:           2
        .value_kind:     hidden_remainder_y
      - .offset:         38
        .size:           2
        .value_kind:     hidden_remainder_z
      - .offset:         56
        .size:           8
        .value_kind:     hidden_global_offset_x
      - .offset:         64
        .size:           8
        .value_kind:     hidden_global_offset_y
      - .offset:         72
        .size:           8
        .value_kind:     hidden_global_offset_z
      - .offset:         80
        .size:           2
        .value_kind:     hidden_grid_dims
    .group_segment_fixed_size: 0
    .kernarg_segment_align: 8
    .kernarg_segment_size: 272
    .language:       OpenCL C
    .language_version:
      - 2
      - 0
    .max_flat_workgroup_size: 1024
    .name:           _Z7prep_w3PKfP15HIP_vector_typeIjLj4EE
    .private_segment_fixed_size: 0
    .sgpr_count:     18
    .sgpr_spill_count: 0
    .symbol:         _Z7prep_w3PKfP15HIP_vector_typeIjLj4EE.kd
    .uniform_work_group_size: 1
    .uses_dynamic_stack: false
    .vgpr_count:     13
    .vgpr_spill_count: 0
    .wavefront_size: 64
  - .agpr_count:     0
    .args:
      - .actual_access:  read_only
        .address_space:  global
        .offset:         0
        .size:           8
        .value_kind:     global_buffer
      - .actual_access:  read_only
        .address_space:  global
        .offset:         8
        .size:           8
        .value_kind:     global_buffer
      - .actual_access:  read_only
        .address_space:  global
        .offset:         16
        .size:           8
        .value_kind:     global_buffer
      - .actual_access:  read_only
        .address_space:  global
        .offset:         24
        .size:           8
        .value_kind:     global_buffer
      - .address_space:  global
        .offset:         32
        .size:           8
        .value_kind:     global_buffer
      - .offset:         40
        .size:           4
        .value_kind:     by_value
      - .offset:         48
        .size:           4
        .value_kind:     hidden_block_count_x
      - .offset:         52
        .size:           4
        .value_kind:     hidden_block_count_y
      - .offset:         56
        .size:           4
        .value_kind:     hidden_block_count_z
      - .offset:         60
        .size:           2
        .value_kind:     hidden_group_size_x
      - .offset:         62
        .size:           2
        .value_kind:     hidden_group_size_y
      - .offset:         64
        .size:           2
        .value_kind:     hidden_group_size_z
      - .offset:         66
        .size:           2
        .value_kind:     hidden_remainder_x
      - .offset:         68
        .size:           2
        .value_kind:     hidden_remainder_y
      - .offset:         70
        .size:           2
        .value_kind:     hidden_remainder_z
      - .offset:         88
        .size:           8
        .value_kind:     hidden_global_offset_x
      - .offset:         96
        .size:           8
        .value_kind:     hidden_global_offset_y
      - .offset:         104
        .size:           8
        .value_kind:     hidden_global_offset_z
      - .offset:         112
        .size:           2
        .value_kind:     hidden_grid_dims
    .group_segment_fixed_size: 25344
    .kernarg_segment_align: 8
    .kernarg_segment_size: 304
    .language:       OpenCL C
    .language_version:
      - 2
      - 0
    .max_flat_workgroup_size: 64
    .name:           _Z7k3_mfmaPK15HIP_vector_typeIjLj4EEPKjS2_PKfPfi
    .private_segment_fixed_size: 0
    .sgpr_count:     52
    .sgpr_spill_count: 0
    .symbol:         _Z7k3_mfmaPK15HIP_vector_typeIjLj4EEPKjS2_PKfPfi.kd
    .uniform_work_group_size: 1
    .uses_dynamic_stack: false
    .vgpr_count:     192
    .vgpr_spill_count: 0
    .wavefront_size: 64
  - .agpr_count:     0
    .args:
      - .actual_access:  read_only
        .address_space:  global
        .offset:         0
        .size:           8
        .value_kind:     global_buffer
      - .actual_access:  read_only
        .address_space:  global
        .offset:         8
        .size:           8
        .value_kind:     global_buffer
      - .actual_access:  read_only
        .address_space:  global
        .offset:         16
        .size:           8
        .value_kind:     global_buffer
      - .actual_access:  write_only
        .address_space:  global
        .offset:         24
        .size:           8
        .value_kind:     global_buffer
      - .actual_access:  write_only
        .address_space:  global
        .offset:         32
        .size:           8
        .value_kind:     global_buffer
      - .actual_access:  read_only
        .address_space:  global
        .offset:         40
        .size:           8
        .value_kind:     global_buffer
      - .actual_access:  read_only
        .address_space:  global
        .offset:         48
        .size:           8
        .value_kind:     global_buffer
      - .actual_access:  read_only
        .address_space:  global
        .offset:         56
        .size:           8
        .value_kind:     global_buffer
      - .actual_access:  write_only
        .address_space:  global
        .offset:         64
        .size:           8
        .value_kind:     global_buffer
      - .actual_access:  write_only
        .address_space:  global
        .offset:         72
        .size:           8
        .value_kind:     global_buffer
    .group_segment_fixed_size: 62848
    .kernarg_segment_align: 8
    .kernarg_segment_size: 80
    .language:       OpenCL C
    .language_version:
      - 2
      - 0
    .max_flat_workgroup_size: 256
    .name:           _Z7k1_mfmaPKfS0_S0_P15HIP_vector_typeIjLj4EEPjS0_S0_S0_S3_S3_
    .private_segment_fixed_size: 0
    .sgpr_count:     28
    .sgpr_spill_count: 0
    .symbol:         _Z7k1_mfmaPKfS0_S0_P15HIP_vector_typeIjLj4EEPjS0_S0_S0_S3_S3_.kd
    .uniform_work_group_size: 1
    .uses_dynamic_stack: false
    .vgpr_count:     170
    .vgpr_spill_count: 0
    .wavefront_size: 64
  - .agpr_count:     0
    .args:
      - .actual_access:  read_only
        .address_space:  global
        .offset:         0
        .size:           8
        .value_kind:     global_buffer
      - .actual_access:  read_only
        .address_space:  global
        .offset:         8
        .size:           8
        .value_kind:     global_buffer
      - .actual_access:  read_only
        .address_space:  global
        .offset:         16
        .size:           8
        .value_kind:     global_buffer
      - .actual_access:  read_only
        .address_space:  global
        .offset:         24
        .size:           8
        .value_kind:     global_buffer
      - .actual_access:  write_only
        .address_space:  global
        .offset:         32
        .size:           8
        .value_kind:     global_buffer
      - .actual_access:  write_only
        .address_space:  global
        .offset:         40
        .size:           8
        .value_kind:     global_buffer
      - .actual_access:  read_only
        .address_space:  global
        .offset:         48
        .size:           8
        .value_kind:     global_buffer
      - .actual_access:  read_only
        .address_space:  global
        .offset:         56
        .size:           8
        .value_kind:     global_buffer
      - .actual_access:  read_only
        .address_space:  global
        .offset:         64
        .size:           8
        .value_kind:     global_buffer
      - .actual_access:  read_only
        .address_space:  global
        .offset:         72
        .size:           8
        .value_kind:     global_buffer
      - .actual_access:  write_only
        .address_space:  global
        .offset:         80
        .size:           8
        .value_kind:     global_buffer
    .group_segment_fixed_size: 0
    .kernarg_segment_align: 8
    .kernarg_segment_size: 88
    .language:       OpenCL C
    .language_version:
      - 2
      - 0
    .max_flat_workgroup_size: 512
    .name:           _Z8k23_mfmaPK15HIP_vector_typeIjLj4EEPKjS2_PKfPS0_PjS2_S4_S2_S6_Pf
    .private_segment_fixed_size: 0
    .sgpr_count:     72
    .sgpr_spill_count: 0
    .symbol:         _Z8k23_mfmaPK15HIP_vector_typeIjLj4EEPKjS2_PKfPS0_PjS2_S4_S2_S6_Pf.kd
    .uniform_work_group_size: 1
    .uses_dynamic_stack: false
    .vgpr_count:     256
    .vgpr_spill_count: 0
    .wavefront_size: 64
  - .agpr_count:     0
    .args:
      - .actual_access:  read_only
        .address_space:  global
        .offset:         0
        .size:           8
        .value_kind:     global_buffer
      - .actual_access:  read_only
        .address_space:  global
        .offset:         8
        .size:           8
        .value_kind:     global_buffer
      - .actual_access:  read_only
        .address_space:  global
        .offset:         16
        .size:           8
        .value_kind:     global_buffer
      - .actual_access:  read_only
        .address_space:  global
        .offset:         24
        .size:           8
        .value_kind:     global_buffer
      - .address_space:  global
        .offset:         32
        .size:           8
        .value_kind:     global_buffer
      - .offset:         40
        .size:           4
        .value_kind:     by_value
    .group_segment_fixed_size: 3240
    .kernarg_segment_align: 8
    .kernarg_segment_size: 44
    .language:       OpenCL C
    .language_version:
      - 2
      - 0
    .max_flat_workgroup_size: 256
    .name:           _Z8k3_naivePK15HIP_vector_typeIjLj4EEPKjPKfS6_Pfi
    .private_segment_fixed_size: 0
    .sgpr_count:     28
    .sgpr_spill_count: 0
    .symbol:         _Z8k3_naivePK15HIP_vector_typeIjLj4EEPKjPKfS6_Pfi.kd
    .uniform_work_group_size: 1
    .uses_dynamic_stack: false
    .vgpr_count:     32
    .vgpr_spill_count: 0
    .wavefront_size: 64
  - .agpr_count:     0
    .args:
      - .actual_access:  read_only
        .address_space:  global
        .offset:         0
        .size:           8
        .value_kind:     global_buffer
      - .actual_access:  read_only
        .address_space:  global
        .offset:         8
        .size:           8
        .value_kind:     global_buffer
      - .actual_access:  read_only
        .address_space:  global
        .offset:         16
        .size:           8
        .value_kind:     global_buffer
      - .actual_access:  read_only
        .address_space:  global
        .offset:         24
        .size:           8
        .value_kind:     global_buffer
      - .address_space:  global
        .offset:         32
        .size:           8
        .value_kind:     global_buffer
      - .offset:         40
        .size:           4
        .value_kind:     hidden_block_count_x
      - .offset:         44
        .size:           4
        .value_kind:     hidden_block_count_y
      - .offset:         48
        .size:           4
        .value_kind:     hidden_block_count_z
      - .offset:         52
        .size:           2
        .value_kind:     hidden_group_size_x
      - .offset:         54
        .size:           2
        .value_kind:     hidden_group_size_y
      - .offset:         56
        .size:           2
        .value_kind:     hidden_group_size_z
      - .offset:         58
        .size:           2
        .value_kind:     hidden_remainder_x
      - .offset:         60
        .size:           2
        .value_kind:     hidden_remainder_y
      - .offset:         62
        .size:           2
        .value_kind:     hidden_remainder_z
      - .offset:         80
        .size:           8
        .value_kind:     hidden_global_offset_x
      - .offset:         88
        .size:           8
        .value_kind:     hidden_global_offset_y
      - .offset:         96
        .size:           8
        .value_kind:     hidden_global_offset_z
      - .offset:         104
        .size:           2
        .value_kind:     hidden_grid_dims
      - .offset:         160
        .size:           4
        .value_kind:     hidden_dynamic_lds_size
    .group_segment_fixed_size: 0
    .kernarg_segment_align: 8
    .kernarg_segment_size: 296
    .language:       OpenCL C
    .language_version:
      - 2
      - 0
    .max_flat_workgroup_size: 512
    .name:           _Z8k3t_mfmaILi1EEvPK15HIP_vector_typeIjLj4EEPKjS3_PKfPf
    .private_segment_fixed_size: 0
    .sgpr_count:     70
    .sgpr_spill_count: 0
    .symbol:         _Z8k3t_mfmaILi1EEvPK15HIP_vector_typeIjLj4EEPKjS3_PKfPf.kd
    .uniform_work_group_size: 1
    .uses_dynamic_stack: false
    .vgpr_count:     238
    .vgpr_spill_count: 0
    .wavefront_size: 64
